# grid barrier, rigorous form of the early invalidate: non-last arrivers invalidate L1 while polling; the XCD's last arriver now waits for its own invalidate to complete BEFORE it releases its XCD
# baseline (speedup 1.0000x reference)
.LBB0_142:
	s_or_b64 exec, exec, s[4:5]
	s_addk_i32 s0, 0x900
	s_mov_b32 s1, 0
	s_lshl_b64 s[0:1], s[0:1], 2
	s_add_u32 s0, s36, s0
	s_addc_u32 s1, s37, s1
	v_mov_b32_e32 v2, 1
	v_mov_b64_e32 v[0:1], s[0:1]
	s_waitcnt vmcnt(0) lgkmcnt(0)
	buffer_inv sc1
	s_waitcnt vmcnt(0)
	flat_atomic_add v[0:1], v2
	s_waitcnt vmcnt(0)

.LBB0_144:
	s_or_b64 exec, exec, s[0:1]
	s_add_i32 s36, s22, 0x900
	s_lshl_b64 s[0:1], s[36:37], 2
	s_add_u32 s0, s60, s0
	s_addc_u32 s1, s61, s1
	v_mov_b64_e32 v[0:1], s[0:1]
	s_waitcnt vmcnt(0) lgkmcnt(0)
	buffer_inv sc1
	s_waitcnt vmcnt(0)
	flat_atomic_add v[0:1], v205
	s_waitcnt vmcnt(0)

.LBB0_273:
	s_or_b64 exec, exec, s[0:1]
	s_add_i32 s36, s22, 0x900
	s_lshl_b64 s[0:1], s[36:37], 2
	s_add_u32 s0, s62, s0
	s_addc_u32 s1, s63, s1
	v_mov_b64_e32 v[0:1], s[0:1]
	s_waitcnt vmcnt(0) lgkmcnt(0)
	buffer_inv sc1
	s_waitcnt vmcnt(0)
	flat_atomic_add v[0:1], v205
	s_waitcnt vmcnt(0)
